# speedup vs baseline: 1.0279x; 1.0104x over previous
.LBB1_13:
	s_or_b64 exec, exec, s[2:3]
	v_div_scale_f32 v66, s[0:1], v101, v101, 1.0
	v_rcp_f32_e32 v67, v66
	v_div_scale_f32 v68, vcc, 1.0, v101, 1.0
	v_fma_f32 v70, -v66, v67, 1.0
	v_fmac_f32_e32 v67, v70, v67
	v_mul_f32_e32 v70, v68, v67
	v_fma_f32 v71, -v66, v70, v68
	v_fmac_f32_e32 v70, v71, v67
	v_fma_f32 v66, -v66, v70, v68
	v_div_fmas_f32 v66, v66, v67, v70
	v_div_fixup_f32 v68, v66, v101, 1.0
	v_lshrrev_b32_e32 v70, 4, v161
	v_and_b32_e32 v71, 15, v161
	v_lshrrev_b32_e32 v72, 3, v164
	v_and_b32_e32 v73, 15, v160
	v_xor_b32_e32 v72, v72, v73
	v_lshlrev_b32_e32 v72, 4, v72
	v_add_u32_e32 v73, v162, v160
	v_lshlrev_b32_e32 v73, 8, v73
	v_add_u32_e32 v73, 0x10000, v73
	v_xor_b32_e32 v74, v71, v70
	v_lshlrev_b32_e32 v74, 4, v74
	v_add_u32_e32 v75, v162, v70
	v_lshlrev_b32_e32 v75, 8, v75
	v_add_u32_e32 v75, 0x10000, v75
	v_or_b32_e32 v64, v64, v70
	v_lshlrev_b64 v[76:77], 8, v[64:65]
	v_lshl_add_u64 v[76:77], v[76:77], 0, s[24:25]
	v_lshlrev_b32_e32 v78, 4, v71
	v_mov_b32_e32 v79, 0
	v_lshl_add_u64 v[76:77], v[76:77], 0, v[78:79]
	s_mov_b64 s[2:3], 0x1000
	v_lshl_add_u64 v[78:79], v[76:77], 0, s[2:3]
	v_mul_f32_e32 v48, v68, v48
	v_mul_f32_e32 v49, v68, v49
	v_mul_f32_e32 v50, v68, v50
	v_mul_f32_e32 v51, v68, v51
	v_mul_f32_e32 v52, v68, v52
	v_mul_f32_e32 v53, v68, v53
	v_mul_f32_e32 v54, v68, v54
	v_mul_f32_e32 v55, v68, v55
	v_cvt_pk_f16_f32 v48, v48, v49
	v_cvt_pk_f16_f32 v49, v50, v51
	v_cvt_pk_f16_f32 v50, v52, v53
	v_cvt_pk_f16_f32 v51, v54, v55
	v_xor_b32_e32 v80, 0x0, v72
	v_add_u32_e32 v80, v80, v73
	v_permlane32_swap_b32_e32 v48, v50
	v_permlane32_swap_b32_e32 v49, v51
	ds_write_b128 v80, v[48:51]
	v_mul_f32_e32 v56, v68, v56
	v_mul_f32_e32 v57, v68, v57
	v_mul_f32_e32 v58, v68, v58
	v_mul_f32_e32 v59, v68, v59
	v_mul_f32_e32 v60, v68, v60
	v_mul_f32_e32 v61, v68, v61
	v_mul_f32_e32 v62, v68, v62
	v_mul_f32_e32 v63, v68, v63
	v_cvt_pk_f16_f32 v56, v56, v57
	v_cvt_pk_f16_f32 v57, v58, v59
	v_cvt_pk_f16_f32 v58, v60, v61
	v_cvt_pk_f16_f32 v59, v62, v63
	v_xor_b32_e32 v80, 0x20, v72
	v_add_u32_e32 v80, v80, v73
	v_permlane32_swap_b32_e32 v56, v58
	v_permlane32_swap_b32_e32 v57, v59
	ds_write_b128 v80, v[56:59]
	v_mul_f32_e32 v32, v68, v32
	v_mul_f32_e32 v33, v68, v33
	v_mul_f32_e32 v34, v68, v34
	v_mul_f32_e32 v35, v68, v35
	v_mul_f32_e32 v36, v68, v36
	v_mul_f32_e32 v37, v68, v37
	v_mul_f32_e32 v38, v68, v38
	v_mul_f32_e32 v39, v68, v39
	v_cvt_pk_f16_f32 v32, v32, v33
	v_cvt_pk_f16_f32 v33, v34, v35
	v_cvt_pk_f16_f32 v34, v36, v37
	v_cvt_pk_f16_f32 v35, v38, v39
	v_xor_b32_e32 v80, 0x40, v72
	v_add_u32_e32 v80, v80, v73
	v_permlane32_swap_b32_e32 v32, v34
	v_permlane32_swap_b32_e32 v33, v35
	ds_write_b128 v80, v[32:35]
	v_mul_f32_e32 v40, v68, v40
	v_mul_f32_e32 v41, v68, v41
	v_mul_f32_e32 v42, v68, v42
	v_mul_f32_e32 v43, v68, v43
	v_mul_f32_e32 v44, v68, v44
	v_mul_f32_e32 v45, v68, v45
	v_mul_f32_e32 v46, v68, v46
	v_mul_f32_e32 v47, v68, v47
	v_cvt_pk_f16_f32 v40, v40, v41
	v_cvt_pk_f16_f32 v41, v42, v43
	v_cvt_pk_f16_f32 v42, v44, v45
	v_cvt_pk_f16_f32 v43, v46, v47
	v_xor_b32_e32 v80, 0x60, v72
	v_add_u32_e32 v80, v80, v73
	v_permlane32_swap_b32_e32 v40, v42
	v_permlane32_swap_b32_e32 v41, v43
	ds_write_b128 v80, v[40:43]
	v_mul_f32_e32 v16, v68, v16
	v_mul_f32_e32 v17, v68, v17
	v_mul_f32_e32 v18, v68, v18
	v_mul_f32_e32 v19, v68, v19
	v_mul_f32_e32 v20, v68, v20
	v_mul_f32_e32 v21, v68, v21
	v_mul_f32_e32 v22, v68, v22
	v_mul_f32_e32 v23, v68, v23
	v_cvt_pk_f16_f32 v16, v16, v17
	v_cvt_pk_f16_f32 v17, v18, v19
	v_cvt_pk_f16_f32 v18, v20, v21
	v_cvt_pk_f16_f32 v19, v22, v23
	v_xor_b32_e32 v80, 0x80, v72
	v_add_u32_e32 v80, v80, v73
	v_permlane32_swap_b32_e32 v16, v18
	v_permlane32_swap_b32_e32 v17, v19
	ds_write_b128 v80, v[16:19]
	v_mul_f32_e32 v24, v68, v24
	v_mul_f32_e32 v25, v68, v25
	v_mul_f32_e32 v26, v68, v26
	v_mul_f32_e32 v27, v68, v27
	v_mul_f32_e32 v28, v68, v28
	v_mul_f32_e32 v29, v68, v29
	v_mul_f32_e32 v30, v68, v30
	v_mul_f32_e32 v31, v68, v31
	v_cvt_pk_f16_f32 v24, v24, v25
	v_cvt_pk_f16_f32 v25, v26, v27
	v_cvt_pk_f16_f32 v26, v28, v29
	v_cvt_pk_f16_f32 v27, v30, v31
	v_xor_b32_e32 v80, 0xa0, v72
	v_add_u32_e32 v80, v80, v73
	v_permlane32_swap_b32_e32 v24, v26
	v_permlane32_swap_b32_e32 v25, v27
	ds_write_b128 v80, v[24:27]
	v_mul_f32_e32 v0, v68, v0
	v_mul_f32_e32 v1, v68, v1
	v_mul_f32_e32 v2, v68, v2
	v_mul_f32_e32 v3, v68, v3
	v_mul_f32_e32 v4, v68, v4
	v_mul_f32_e32 v5, v68, v5
	v_mul_f32_e32 v6, v68, v6
	v_mul_f32_e32 v7, v68, v7
	v_cvt_pk_f16_f32 v0, v0, v1
	v_cvt_pk_f16_f32 v1, v2, v3
	v_cvt_pk_f16_f32 v2, v4, v5
	v_cvt_pk_f16_f32 v3, v6, v7
	v_xor_b32_e32 v80, 0xc0, v72
	v_add_u32_e32 v80, v80, v73
	v_permlane32_swap_b32_e32 v0, v2
	v_permlane32_swap_b32_e32 v1, v3
	ds_write_b128 v80, v[0:3]
	v_mul_f32_e32 v8, v68, v8
	v_mul_f32_e32 v9, v68, v9
	v_mul_f32_e32 v10, v68, v10
	v_mul_f32_e32 v11, v68, v11
	v_mul_f32_e32 v12, v68, v12
	v_mul_f32_e32 v13, v68, v13
	v_mul_f32_e32 v14, v68, v14
	v_mul_f32_e32 v15, v68, v15
	v_cvt_pk_f16_f32 v8, v8, v9
	v_cvt_pk_f16_f32 v9, v10, v11
	v_cvt_pk_f16_f32 v10, v12, v13
	v_cvt_pk_f16_f32 v11, v14, v15
	v_xor_b32_e32 v80, 0xe0, v72
	v_add_u32_e32 v80, v80, v73
	v_permlane32_swap_b32_e32 v8, v10
	v_permlane32_swap_b32_e32 v9, v11
	ds_write_b128 v80, v[8:11]
	s_waitcnt lgkmcnt(0)
	v_xor_b32_e32 v81, 0x0, v74
	v_add_u32_e32 v81, v81, v75
	ds_read_b128 v[88:91], v81 offset:0
	v_xor_b32_e32 v81, 0x40, v74
	v_add_u32_e32 v81, v81, v75
	ds_read_b128 v[92:95], v81 offset:1024
	v_xor_b32_e32 v81, 0x80, v74
	v_add_u32_e32 v81, v81, v75
	ds_read_b128 v[96:99], v81 offset:2048
	v_xor_b32_e32 v81, 0xc0, v74
	v_add_u32_e32 v81, v81, v75
	ds_read_b128 v[100:103], v81 offset:3072
	v_xor_b32_e32 v81, 0x0, v74
	v_add_u32_e32 v81, v81, v75
	ds_read_b128 v[104:107], v81 offset:4096
	v_xor_b32_e32 v81, 0x40, v74
	v_add_u32_e32 v81, v81, v75
	ds_read_b128 v[108:111], v81 offset:5120
	v_xor_b32_e32 v81, 0x80, v74
	v_add_u32_e32 v81, v81, v75
	ds_read_b128 v[112:115], v81 offset:6144
	v_xor_b32_e32 v81, 0xc0, v74
	v_add_u32_e32 v81, v81, v75
	ds_read_b128 v[116:119], v81 offset:7168
	s_waitcnt lgkmcnt(7)
	global_store_dwordx4 v[76:77], v[88:91], off offset:0 sc1
	s_waitcnt lgkmcnt(6)
	global_store_dwordx4 v[76:77], v[92:95], off offset:1024 sc1
	s_waitcnt lgkmcnt(5)
	global_store_dwordx4 v[76:77], v[96:99], off offset:2048 sc1
	s_waitcnt lgkmcnt(4)
	global_store_dwordx4 v[76:77], v[100:103], off offset:3072 sc1
	s_waitcnt lgkmcnt(3)
	global_store_dwordx4 v[78:79], v[104:107], off offset:0 sc1
	s_waitcnt lgkmcnt(2)
	global_store_dwordx4 v[78:79], v[108:111], off offset:1024 sc1
	s_waitcnt lgkmcnt(1)
	global_store_dwordx4 v[78:79], v[112:115], off offset:2048 sc1
	s_waitcnt lgkmcnt(0)
	global_store_dwordx4 v[78:79], v[116:119], off offset:3072 sc1
	s_endpgm
